# conversion tickets 2-of-5 in layers 1,2 (layer 0 at 1-of-2): second measurement of v52
# speedup vs baseline: 1.0129x; 1.0012x over previous
.LBB0_789:
	s_or_b64 exec, exec, s[2:3]
	v_readlane_b32 s2, v253, 55
	s_waitcnt lgkmcnt(0)
	s_barrier
	v_mov_b32_e32 v0, s2
	v_readlane_b32 s2, v253, 54
	ds_read_b32 v0, v0
	s_nop 0
	v_mov_b32_e32 v1, s2
	ds_read_b32 v1, v1
	s_waitcnt lgkmcnt(0)
	s_barrier
	v_add_u32_e32 v201, 0x580, v0
	s_nop 0
	v_readfirstlane_b32 s100, v201
	v_readlane_b32 s101, v254, 38
	s_nop 3
	s_movk_i32 vcc_lo, 0x4c0
	s_movk_i32 vcc_hi, 0xbe0
	s_cmp_eq_u32 s101, 0
	s_cselect_b32 vcc_lo, 0xac0, vcc_lo
	s_cselect_b32 vcc_hi, 0x1580, vcc_hi
	s_cmp_eq_u32 s101, 3
	s_cselect_b32 vcc_lo, 0, vcc_lo
	s_cselect_b32 vcc_hi, 0, vcc_hi
	s_add_i32 vcc_lo, s100, vcc_lo
	s_max_u32 vcc_lo, vcc_lo, vcc_hi
	v_mov_b32_e32 v201, vcc_lo
	v_readfirstlane_b32 s30, v0
	v_cmp_ge_i32_e32 vcc, v1, v201
	v_readfirstlane_b32 s24, v1
	s_cbranch_vccnz .LBB0_931
	s_add_u32 s31, s4, 0x37b00000
	s_addc_u32 s34, s5, 0
	s_add_i32 s35, s30, 0x480
	s_add_u32 s44, s4, 0x61800000
	s_addc_u32 s45, s5, 0
	s_add_u32 s46, s4, 0x42c00000
	s_addc_u32 s47, s5, 0
	s_add_u32 s10, s4, 0x66d00000
	s_addc_u32 s11, s5, 0
	s_add_u32 s48, s4, 0x61640000
	s_movk_i32 s2, 0x100
	s_addc_u32 s49, s5, 0
	v_cmp_gt_i32_e64 s[38:39], s2, v199
	s_add_i32 s2, 0, 0x14800
	v_add_u32_e32 v214, s2, v200
	s_add_i32 s2, 0, 0x16800
	s_cmp_lg_u32 0, -1
	v_lshlrev_b32_e32 v3, 1, v199
	v_lshlrev_b32_e32 v211, 4, v199
	s_cselect_b32 s3, 0, 0
	v_lshlrev_b32_e32 v0, 3, v199
	v_lshlrev_b32_e32 v1, 10, v101
	v_lshlrev_b32_e32 v2, 4, v198
	v_and_b32_e32 v3, 32, v3
	v_and_b32_e32 v5, 0xc0, v211
	s_addk_i32 s3, 0x6000
	v_and_b32_e32 v210, 24, v0
	v_lshl_or_b32 v5, v101, 8, v5
	v_add3_u32 v213, 0, v1, v2
	v_add_u32_e32 v1, s3, v3
	v_add3_u32 v217, v1, v210, v5
	v_lshrrev_b32_e32 v1, 3, v100
	v_lshl_add_u32 v215, v198, 2, s2
	v_and_b32_e32 v218, 56, v0
	v_lshl_add_u32 v220, v1, 2, s2
	s_add_i32 s2, 0, 0x14a00
	v_add_u32_e32 v4, 0, v3
	v_lshlrev_b32_e32 v96, 1, v218
	v_add_u32_e32 v221, s2, v200
	s_add_i32 s2, 0, 0x14900
	v_ashrrev_i32_e32 v203, 31, v202
	v_lshlrev_b32_e32 v208, 9, v100
	v_lshrrev_b32_e32 v209, 2, v100
	v_add3_u32 v212, v4, v210, v5
	v_cmp_gt_u32_e64 s[40:41], 32, v100
	v_cmp_lt_u32_e64 s[42:43], 31, v100
	v_or_b32_e32 v216, 0xc0, v206
	v_lshl_add_u64 v[204:205], s[4:5], 0, v[96:97]
	v_lshlrev_b32_e32 v219, 7, v1
	v_add_u32_e32 v222, s2, v200
	v_lshlrev_b32_e32 v96, 1, v98
	s_branch .LBB0_792
